# L1: GEMM workgroup b<256 continues with tile b+256 in-kernel (no s_endpgm store drain / re-dispatch between tiles); workgroups 256-511 exit at once
# speedup vs baseline: 1.0206x; 1.0036x over previous
_Z16gemm_glds_kernelILi2EEvPKDF16_PDF16_PKiS4_S1_S1_PKfiS6_Pc:
	s_mov_b64 s[44:45], s[0:1]
	s_mov_b32 s46, s2
	s_mov_b32 s47, 0
	v_mov_b32_e32 v186, v0
	s_load_dword s3, s[0:1], 0x38
	s_mov_b64 s[4:5], -1
	s_waitcnt lgkmcnt(0)
	s_cmp_lt_i32 s2, s3
	s_cbranch_scc1 .LBB2_2
	s_sub_i32 s3, s2, s3
	s_cmp_gt_u32 s3, 255
	s_cbranch_scc1 .LBB2_14
	s_load_dwordx4 s[4:7], s[0:1], 0x40
	v_lshrrev_b32_e32 v1, 8, v0
	v_and_b32_e32 v2, 0xff, v0
	v_and_b32_e32 v3, 63, v0
	v_readfirstlane_b32 s8, v1
	v_bfe_u32 v4, v0, 6, 2
	s_lshl_b32 s9, s3, 1
	s_nop 1
	s_add_u32 s9, s9, s8
	s_lshr_b32 s10, s9, 8
	s_bfe_u32 s11, s9, 0x40004
	s_and_b32 s12, s9, 15
	s_lshl_b32 s13, s11, 6
	s_lshl_b32 s14, s12, 6
	s_mul_i32 s15, s10, 0x3d2844
	s_movk_i32 s24, 0x3e9
	s_waitcnt lgkmcnt(0)
	s_add_u32 s16, s4, s15
	s_addc_u32 s17, s5, 0
	s_add_u32 s18, s16, 0x7a5088
	s_addc_u32 s19, s17, 0
	s_lshl_b32 s15, s10, 21
	s_add_u32 s20, s6, s15
	s_addc_u32 s21, s7, 0
	s_add_u32 s20, s20, 0x800000
	s_addc_u32 s21, s21, 0
	s_add_u32 s22, s20, 0x400000
	s_addc_u32 s23, s21, 0
	v_add_u32_e32 v5, s13, v4
	v_add_u32_e32 v6, s14, v3
	v_cmp_gt_u32_e64 s[28:29], s24, v6
	v_min_u32_e32 v6, 0x3e8, v6
	v_lshlrev_b32_e32 v6, 2, v6
	v_min_u32_e32 v7, 0x3e8, v5
	v_mul_u32_u24_e32 v7, 0xfa4, v7
	v_add_u32_e32 v48, v7, v6
	v_add_u32_e32 v7, 4, v5
	v_min_u32_e32 v7, 0x3e8, v7
	v_mul_u32_u24_e32 v7, 0xfa4, v7
	v_add_u32_e32 v49, v7, v6
	v_add_u32_e32 v7, 8, v5
	v_min_u32_e32 v7, 0x3e8, v7
	v_mul_u32_u24_e32 v7, 0xfa4, v7
	v_add_u32_e32 v50, v7, v6
	v_add_u32_e32 v7, 12, v5
	v_min_u32_e32 v7, 0x3e8, v7
	v_mul_u32_u24_e32 v7, 0xfa4, v7
	v_add_u32_e32 v51, v7, v6
	v_add_u32_e32 v7, 16, v5
	v_min_u32_e32 v7, 0x3e8, v7
	v_mul_u32_u24_e32 v7, 0xfa4, v7
	v_add_u32_e32 v52, v7, v6
	v_add_u32_e32 v7, 20, v5
	v_min_u32_e32 v7, 0x3e8, v7
	v_mul_u32_u24_e32 v7, 0xfa4, v7
	v_add_u32_e32 v53, v7, v6
	v_add_u32_e32 v7, 24, v5
	v_min_u32_e32 v7, 0x3e8, v7
	v_mul_u32_u24_e32 v7, 0xfa4, v7
	v_add_u32_e32 v54, v7, v6
	v_add_u32_e32 v7, 28, v5
	v_min_u32_e32 v7, 0x3e8, v7
	v_mul_u32_u24_e32 v7, 0xfa4, v7
	v_add_u32_e32 v55, v7, v6
	v_add_u32_e32 v7, 32, v5
	v_min_u32_e32 v7, 0x3e8, v7
	v_mul_u32_u24_e32 v7, 0xfa4, v7
	v_add_u32_e32 v56, v7, v6
	v_add_u32_e32 v7, 36, v5
	v_min_u32_e32 v7, 0x3e8, v7
	v_mul_u32_u24_e32 v7, 0xfa4, v7
	v_add_u32_e32 v57, v7, v6
	v_add_u32_e32 v7, 40, v5
	v_min_u32_e32 v7, 0x3e8, v7
	v_mul_u32_u24_e32 v7, 0xfa4, v7
	v_add_u32_e32 v58, v7, v6
	v_add_u32_e32 v7, 44, v5
	v_min_u32_e32 v7, 0x3e8, v7
	v_mul_u32_u24_e32 v7, 0xfa4, v7
	v_add_u32_e32 v59, v7, v6
	v_add_u32_e32 v7, 48, v5
	v_min_u32_e32 v7, 0x3e8, v7
	v_mul_u32_u24_e32 v7, 0xfa4, v7
	v_add_u32_e32 v60, v7, v6
	v_add_u32_e32 v7, 52, v5
	v_min_u32_e32 v7, 0x3e8, v7
	v_mul_u32_u24_e32 v7, 0xfa4, v7
	v_add_u32_e32 v61, v7, v6
	v_add_u32_e32 v7, 56, v5
	v_min_u32_e32 v7, 0x3e8, v7
	v_mul_u32_u24_e32 v7, 0xfa4, v7
	v_add_u32_e32 v62, v7, v6
	v_add_u32_e32 v7, 60, v5
	v_min_u32_e32 v7, 0x3e8, v7
	v_mul_u32_u24_e32 v7, 0xfa4, v7
	v_add_u32_e32 v63, v7, v6
	global_load_dword v16, v48, s[16:17] nt
	global_load_dword v17, v49, s[16:17] nt
	global_load_dword v18, v50, s[16:17] nt
	global_load_dword v19, v51, s[16:17] nt
	global_load_dword v20, v52, s[16:17] nt
	global_load_dword v21, v53, s[16:17] nt
	global_load_dword v22, v54, s[16:17] nt
	global_load_dword v23, v55, s[16:17] nt
	global_load_dword v24, v56, s[16:17] nt
	global_load_dword v25, v57, s[16:17] nt
	global_load_dword v26, v58, s[16:17] nt
	global_load_dword v27, v59, s[16:17] nt
	global_load_dword v28, v60, s[16:17] nt
	global_load_dword v29, v61, s[16:17] nt
	global_load_dword v30, v62, s[16:17] nt
	global_load_dword v31, v63, s[16:17] nt
	global_load_dword v32, v48, s[18:19] nt
	global_load_dword v33, v49, s[18:19] nt
	global_load_dword v34, v50, s[18:19] nt
	global_load_dword v35, v51, s[18:19] nt
	global_load_dword v36, v52, s[18:19] nt
	global_load_dword v37, v53, s[18:19] nt
	global_load_dword v38, v54, s[18:19] nt
	global_load_dword v39, v55, s[18:19] nt
	global_load_dword v40, v56, s[18:19] nt
	global_load_dword v41, v57, s[18:19] nt
	global_load_dword v42, v58, s[18:19] nt
	global_load_dword v43, v59, s[18:19] nt
	global_load_dword v44, v60, s[18:19] nt
	global_load_dword v45, v61, s[18:19] nt
	global_load_dword v46, v62, s[18:19] nt
	global_load_dword v47, v63, s[18:19] nt
	v_mul_u32_u24_e32 v8, 65, v4
	v_add_u32_e32 v8, v8, v3
	v_lshlrev_b32_e32 v8, 2, v8
	s_mul_i32 s25, s8, 0x4100
	v_add_u32_e32 v8, s25, v8
	v_and_b32_e32 v9, 7, v2
	v_lshrrev_b32_e32 v10, 3, v2
	v_mul_u32_u24_e32 v11, 0x208, v9
	v_add_u32_e32 v11, v11, v10
	v_lshlrev_b32_e32 v11, 2, v11
	v_add_u32_e32 v11, s25, v11
	v_add_u32_e32 v12, s14, v10
	v_lshlrev_b32_e32 v12, 11, v12
	v_lshlrev_b32_e32 v13, 4, v9
	v_add_u32_e32 v12, v12, v13
	s_lshl_b32 s26, s13, 1
	v_add_u32_e32 v12, s26, v12
	v_add_u32_e32 v14, 0x10000, v12
	s_waitcnt vmcnt(31)
	v_cmp_gt_u32_e32 vcc, s24, v5
	s_and_b64 vcc, vcc, s[28:29]
	s_nop 1
	v_cndmask_b32_e32 v7, 0, v16, vcc
	ds_write_b32 v8, v7
	s_waitcnt vmcnt(30)
	v_add_u32_e32 v7, 4, v5
	v_cmp_gt_u32_e32 vcc, s24, v7
	s_and_b64 vcc, vcc, s[28:29]
	s_nop 1
	v_cndmask_b32_e32 v7, 0, v17, vcc
	ds_write_b32 v8, v7 offset:1040
	s_waitcnt vmcnt(29)
	v_add_u32_e32 v7, 8, v5
	v_cmp_gt_u32_e32 vcc, s24, v7
	s_and_b64 vcc, vcc, s[28:29]
	s_nop 1
	v_cndmask_b32_e32 v7, 0, v18, vcc
	ds_write_b32 v8, v7 offset:2080
	s_waitcnt vmcnt(28)
	v_add_u32_e32 v7, 12, v5
	v_cmp_gt_u32_e32 vcc, s24, v7
	s_and_b64 vcc, vcc, s[28:29]
	s_nop 1
	v_cndmask_b32_e32 v7, 0, v19, vcc
	ds_write_b32 v8, v7 offset:3120
	s_waitcnt vmcnt(27)
	v_add_u32_e32 v7, 16, v5
	v_cmp_gt_u32_e32 vcc, s24, v7
	s_and_b64 vcc, vcc, s[28:29]
	s_nop 1
	v_cndmask_b32_e32 v7, 0, v20, vcc
	ds_write_b32 v8, v7 offset:4160
	s_waitcnt vmcnt(26)
	v_add_u32_e32 v7, 20, v5
	v_cmp_gt_u32_e32 vcc, s24, v7
	s_and_b64 vcc, vcc, s[28:29]
	s_nop 1
	v_cndmask_b32_e32 v7, 0, v21, vcc
	ds_write_b32 v8, v7 offset:5200
	s_waitcnt vmcnt(25)
	v_add_u32_e32 v7, 24, v5
	v_cmp_gt_u32_e32 vcc, s24, v7
	s_and_b64 vcc, vcc, s[28:29]
	s_nop 1
	v_cndmask_b32_e32 v7, 0, v22, vcc
	ds_write_b32 v8, v7 offset:6240
	s_waitcnt vmcnt(24)
	v_add_u32_e32 v7, 28, v5
	v_cmp_gt_u32_e32 vcc, s24, v7
	s_and_b64 vcc, vcc, s[28:29]
	s_nop 1
	v_cndmask_b32_e32 v7, 0, v23, vcc
	ds_write_b32 v8, v7 offset:7280
	s_waitcnt vmcnt(23)
	v_add_u32_e32 v7, 32, v5
	v_cmp_gt_u32_e32 vcc, s24, v7
	s_and_b64 vcc, vcc, s[28:29]
	s_nop 1
	v_cndmask_b32_e32 v7, 0, v24, vcc
	ds_write_b32 v8, v7 offset:8320
	s_waitcnt vmcnt(22)
	v_add_u32_e32 v7, 36, v5
	v_cmp_gt_u32_e32 vcc, s24, v7
	s_and_b64 vcc, vcc, s[28:29]
	s_nop 1
	v_cndmask_b32_e32 v7, 0, v25, vcc
	ds_write_b32 v8, v7 offset:9360
	s_waitcnt vmcnt(21)
	v_add_u32_e32 v7, 40, v5
	v_cmp_gt_u32_e32 vcc, s24, v7
	s_and_b64 vcc, vcc, s[28:29]
	s_nop 1
	v_cndmask_b32_e32 v7, 0, v26, vcc
	ds_write_b32 v8, v7 offset:10400
	s_waitcnt vmcnt(20)
	v_add_u32_e32 v7, 44, v5
	v_cmp_gt_u32_e32 vcc, s24, v7
	s_and_b64 vcc, vcc, s[28:29]
	s_nop 1
	v_cndmask_b32_e32 v7, 0, v27, vcc
	ds_write_b32 v8, v7 offset:11440
	s_waitcnt vmcnt(19)
	v_add_u32_e32 v7, 48, v5
	v_cmp_gt_u32_e32 vcc, s24, v7
	s_and_b64 vcc, vcc, s[28:29]
	s_nop 1
	v_cndmask_b32_e32 v7, 0, v28, vcc
	ds_write_b32 v8, v7 offset:12480
	s_waitcnt vmcnt(18)
	v_add_u32_e32 v7, 52, v5
	v_cmp_gt_u32_e32 vcc, s24, v7
	s_and_b64 vcc, vcc, s[28:29]
	s_nop 1
	v_cndmask_b32_e32 v7, 0, v29, vcc
	ds_write_b32 v8, v7 offset:13520
	s_waitcnt vmcnt(17)
	v_add_u32_e32 v7, 56, v5
	v_cmp_gt_u32_e32 vcc, s24, v7
	s_and_b64 vcc, vcc, s[28:29]
	s_nop 1
	v_cndmask_b32_e32 v7, 0, v30, vcc
	ds_write_b32 v8, v7 offset:14560
	s_waitcnt vmcnt(16)
	v_add_u32_e32 v7, 60, v5
	v_cmp_gt_u32_e32 vcc, s24, v7
	s_and_b64 vcc, vcc, s[28:29]
	s_nop 1
	v_cndmask_b32_e32 v7, 0, v31, vcc
	ds_write_b32 v8, v7 offset:15600
	s_waitcnt lgkmcnt(0)
	s_barrier
	ds_read_b32 v64, v11
	ds_read_b32 v65, v11 offset:260
	ds_read_b32 v66, v11 offset:520
	ds_read_b32 v67, v11 offset:780
	ds_read_b32 v68, v11 offset:1040
	ds_read_b32 v69, v11 offset:1300
	ds_read_b32 v70, v11 offset:1560
	ds_read_b32 v71, v11 offset:1820
	ds_read_b32 v72, v11 offset:128
	ds_read_b32 v73, v11 offset:388
	ds_read_b32 v74, v11 offset:648
	ds_read_b32 v75, v11 offset:908
	s_waitcnt lgkmcnt(4)
	ds_read_b32 v76, v11 offset:1168
	ds_read_b32 v77, v11 offset:1428
	ds_read_b32 v78, v11 offset:1688
	ds_read_b32 v79, v11 offset:1948
	s_waitcnt lgkmcnt(0)
	v_cvt_pk_f16_f32 v80, v64, v65
	v_cvt_pk_f16_f32 v81, v66, v67
	v_cvt_pk_f16_f32 v82, v68, v69
	v_cvt_pk_f16_f32 v83, v70, v71
	v_cvt_pk_f16_f32 v84, v72, v73
	v_cvt_pk_f16_f32 v85, v74, v75
	v_cvt_pk_f16_f32 v86, v76, v77
	v_cvt_pk_f16_f32 v87, v78, v79
	global_store_dwordx4 v12, v[80:83], s[20:21]
	global_store_dwordx4 v14, v[84:87], s[20:21]
	s_barrier
	s_waitcnt vmcnt(17)
	v_cmp_gt_u32_e32 vcc, s24, v5
	s_and_b64 vcc, vcc, s[28:29]
	s_nop 1
	v_cndmask_b32_e32 v7, 0, v32, vcc
	ds_write_b32 v8, v7
	s_waitcnt vmcnt(16)
	v_add_u32_e32 v7, 4, v5
	v_cmp_gt_u32_e32 vcc, s24, v7
	s_and_b64 vcc, vcc, s[28:29]
	s_nop 1
	v_cndmask_b32_e32 v7, 0, v33, vcc
	ds_write_b32 v8, v7 offset:1040
	s_waitcnt vmcnt(15)
	v_add_u32_e32 v7, 8, v5
	v_cmp_gt_u32_e32 vcc, s24, v7
	s_and_b64 vcc, vcc, s[28:29]
	s_nop 1
	v_cndmask_b32_e32 v7, 0, v34, vcc
	ds_write_b32 v8, v7 offset:2080
	s_waitcnt vmcnt(14)
	v_add_u32_e32 v7, 12, v5
	v_cmp_gt_u32_e32 vcc, s24, v7
	s_and_b64 vcc, vcc, s[28:29]
	s_nop 1
	v_cndmask_b32_e32 v7, 0, v35, vcc
	ds_write_b32 v8, v7 offset:3120
	s_waitcnt vmcnt(13)
	v_add_u32_e32 v7, 16, v5
	v_cmp_gt_u32_e32 vcc, s24, v7
	s_and_b64 vcc, vcc, s[28:29]
	s_nop 1
	v_cndmask_b32_e32 v7, 0, v36, vcc
	ds_write_b32 v8, v7 offset:4160
	s_waitcnt vmcnt(12)
	v_add_u32_e32 v7, 20, v5
	v_cmp_gt_u32_e32 vcc, s24, v7
	s_and_b64 vcc, vcc, s[28:29]
	s_nop 1
	v_cndmask_b32_e32 v7, 0, v37, vcc
	ds_write_b32 v8, v7 offset:5200
	s_waitcnt vmcnt(11)
	v_add_u32_e32 v7, 24, v5
	v_cmp_gt_u32_e32 vcc, s24, v7
	s_and_b64 vcc, vcc, s[28:29]
	s_nop 1
	v_cndmask_b32_e32 v7, 0, v38, vcc
	ds_write_b32 v8, v7 offset:6240
	s_waitcnt vmcnt(10)
	v_add_u32_e32 v7, 28, v5
	v_cmp_gt_u32_e32 vcc, s24, v7
	s_and_b64 vcc, vcc, s[28:29]
	s_nop 1
	v_cndmask_b32_e32 v7, 0, v39, vcc
	ds_write_b32 v8, v7 offset:7280
	s_waitcnt vmcnt(9)
	v_add_u32_e32 v7, 32, v5
	v_cmp_gt_u32_e32 vcc, s24, v7
	s_and_b64 vcc, vcc, s[28:29]
	s_nop 1
	v_cndmask_b32_e32 v7, 0, v40, vcc
	ds_write_b32 v8, v7 offset:8320
	s_waitcnt vmcnt(8)
	v_add_u32_e32 v7, 36, v5
	v_cmp_gt_u32_e32 vcc, s24, v7
	s_and_b64 vcc, vcc, s[28:29]
	s_nop 1
	v_cndmask_b32_e32 v7, 0, v41, vcc
	ds_write_b32 v8, v7 offset:9360
	s_waitcnt vmcnt(7)
	v_add_u32_e32 v7, 40, v5
	v_cmp_gt_u32_e32 vcc, s24, v7
	s_and_b64 vcc, vcc, s[28:29]
	s_nop 1
	v_cndmask_b32_e32 v7, 0, v42, vcc
	ds_write_b32 v8, v7 offset:10400
	s_waitcnt vmcnt(6)
	v_add_u32_e32 v7, 44, v5
	v_cmp_gt_u32_e32 vcc, s24, v7
	s_and_b64 vcc, vcc, s[28:29]
	s_nop 1
	v_cndmask_b32_e32 v7, 0, v43, vcc
	ds_write_b32 v8, v7 offset:11440
	s_waitcnt vmcnt(5)
	v_add_u32_e32 v7, 48, v5
	v_cmp_gt_u32_e32 vcc, s24, v7
	s_and_b64 vcc, vcc, s[28:29]
	s_nop 1
	v_cndmask_b32_e32 v7, 0, v44, vcc
	ds_write_b32 v8, v7 offset:12480
	s_waitcnt vmcnt(4)
	v_add_u32_e32 v7, 52, v5
	v_cmp_gt_u32_e32 vcc, s24, v7
	s_and_b64 vcc, vcc, s[28:29]
	s_nop 1
	v_cndmask_b32_e32 v7, 0, v45, vcc
	ds_write_b32 v8, v7 offset:13520
	s_waitcnt vmcnt(3)
	v_add_u32_e32 v7, 56, v5
	v_cmp_gt_u32_e32 vcc, s24, v7
	s_and_b64 vcc, vcc, s[28:29]
	s_nop 1
	v_cndmask_b32_e32 v7, 0, v46, vcc
	ds_write_b32 v8, v7 offset:14560
	s_waitcnt vmcnt(2)
	v_add_u32_e32 v7, 60, v5
	v_cmp_gt_u32_e32 vcc, s24, v7
	s_and_b64 vcc, vcc, s[28:29]
	s_nop 1
	v_cndmask_b32_e32 v7, 0, v47, vcc
	ds_write_b32 v8, v7 offset:15600
	s_waitcnt lgkmcnt(0)
	s_barrier
	ds_read_b32 v64, v11
	ds_read_b32 v65, v11 offset:260
	ds_read_b32 v66, v11 offset:520
	ds_read_b32 v67, v11 offset:780
	ds_read_b32 v68, v11 offset:1040
	ds_read_b32 v69, v11 offset:1300
	ds_read_b32 v70, v11 offset:1560
	ds_read_b32 v71, v11 offset:1820
	ds_read_b32 v72, v11 offset:128
	ds_read_b32 v73, v11 offset:388
	ds_read_b32 v74, v11 offset:648
	ds_read_b32 v75, v11 offset:908
	s_waitcnt lgkmcnt(4)
	ds_read_b32 v76, v11 offset:1168
	ds_read_b32 v77, v11 offset:1428
	ds_read_b32 v78, v11 offset:1688
	ds_read_b32 v79, v11 offset:1948
	s_waitcnt lgkmcnt(0)
	v_cvt_pk_f16_f32 v80, v64, v65
	v_cvt_pk_f16_f32 v81, v66, v67
	v_cvt_pk_f16_f32 v82, v68, v69
	v_cvt_pk_f16_f32 v83, v70, v71
	v_cvt_pk_f16_f32 v84, v72, v73
	v_cvt_pk_f16_f32 v85, v74, v75
	v_cvt_pk_f16_f32 v86, v76, v77
	v_cvt_pk_f16_f32 v87, v78, v79
	global_store_dwordx4 v12, v[80:83], s[22:23]
	global_store_dwordx4 v14, v[84:87], s[22:23]
	s_branch .LBB2_14
.LBB2_2:
	s_andn2_b64 vcc, exec, s[4:5]
	s_cbranch_vccnz .LBB2_14
	s_cmp_lg_u32 s47, 0
	s_cbranch_scc1 .Lch_go
	s_sub_u32 s35, s2, 0x100
	s_cmp_lt_u32 s35, 0x100
	s_cbranch_scc1 .LBB2_14
.Lch_go:
	s_ashr_i32 s16, s2, 3
	s_lshr_b32 s3, s16, 30
	s_add_i32 s3, s16, s3
	s_load_dwordx2 s[4:5], s[0:1], 0x18
	s_load_dwordx2 s[18:19], s[0:1], 0x10
	s_load_dwordx4 s[8:11], s[0:1], 0x20
	s_load_dwordx2 s[12:13], s[0:1], 0x30
	s_ashr_i32 s17, s3, 2
	s_lshl_b32 s3, s17, 3
	s_and_b32 s2, s2, 7
	s_or_b32 s2, s3, s2
	s_ashr_i32 s3, s2, 31
	s_lshl_b64 s[6:7], s[2:3], 2
	v_readfirstlane_b32 s35, v0
	v_bfe_u32 v3, v0, 3, 3
	s_nop 2
	s_lshr_b32 s21, s35, 6
	v_lshl_or_b32 v5, s21, 4, v3
	v_lshlrev_b32_e32 v1, 2, v5
	s_lshl_b32 s36, s2, 7
	s_ashr_i32 s37, s36, 31
	s_lshl_b64 s[36:37], s[36:37], 2
	s_waitcnt lgkmcnt(0)
	s_add_u32 s4, s4, s6
	s_addc_u32 s5, s5, s7
	s_load_dword s15, s[4:5], 0x0
	s_add_u32 s36, s18, s36
	s_addc_u32 s37, s19, s37
	global_load_dword v2, v1, s[36:37]
	global_load_dword v4, v1, s[36:37] offset:32
	v_and_b32_e32 v1, 15, v0
	s_lshr_b32 s23, s35, 8
	v_lshl_or_b32 v83, s23, 6, v1
	v_lshlrev_b32_e32 v10, 2, v83
	global_load_dword v88, v10, s[36:37]
	global_load_dword v86, v10, s[36:37] offset:64
	global_load_dword v84, v10, s[36:37] offset:128
	global_load_dword v82, v10, s[36:37] offset:192
	s_mov_b32 s14, 0
	s_waitcnt lgkmcnt(0)
	s_cmp_lt_i32 s15, 0
	s_cbranch_scc1 .LBB2_14
	s_lshl_b32 s2, s2, 7
	s_ashr_i32 s3, s2, 31
	s_lshl_b64 s[2:3], s[2:3], 2
	s_add_u32 s2, s18, s2
	s_load_dwordx4 s[4:7], s[0:1], 0x0
	s_addc_u32 s3, s19, s3
	s_lshl_b32 s0, s17, 2
	s_and_b32 s18, s15, 0xff
	s_sub_i32 s0, s16, s0
	s_lshl_b32 s1, s18, 21
	s_add_u32 s19, s8, s1
	v_readfirstlane_b32 s1, v0
	s_addc_u32 s20, s9, 0
	s_lshr_b32 s21, s1, 6
	v_bfe_u32 v3, v0, 3, 3
	v_lshl_or_b32 v5, s21, 4, v3
	v_lshlrev_b32_e32 v1, 2, v5
	s_bfe_u32 s22, s1, 0x20006
	s_lshl_b32 s8, s18, 12
	s_add_u32 s12, s12, s8
	s_addc_u32 s13, s13, 0
	s_lshl_b32 s0, s0, 8
	v_and_b32_e32 v1, 15, v0
	s_lshr_b32 s23, s1, 8
	s_ashr_i32 s1, s0, 31
	v_lshl_or_b32 v83, s23, 6, v1
	s_lshl_b64 s[8:9], s[0:1], 2
	v_lshlrev_b32_e32 v10, 2, v83
	s_add_u32 s12, s12, s8
	s_addc_u32 s2, s13, s9
	s_lshl_b32 s8, s22, 6
	s_lshl_b32 s3, s22, 8
	v_lshrrev_b32_e32 v44, 1, v5
	s_add_u32 s16, s12, s3
	v_lshl_or_b32 v13, s21, 5, v3
	v_or_b32_e32 v3, 8, v5
	v_xor_b32_e32 v7, v44, v0
	s_addc_u32 s17, s2, 0
	s_lshl_b32 s9, s21, 11
	s_lshl_b32 s12, s21, 12
	v_or_b32_e32 v5, 8, v13
	v_lshrrev_b32_e32 v45, 1, v3
	v_lshlrev_b32_e32 v3, 4, v7
	s_add_i32 s13, s9, 0
	s_add_i32 s2, s12, 0
	v_lshrrev_b32_e32 v46, 1, v5
	v_add_u32_e32 v8, s0, v5
	v_xor_b32_e32 v5, v45, v0
	v_and_b32_e32 v18, 0x70, v3
	s_add_i32 s21, s13, 0x400
	s_add_i32 s24, s2, 0x4000
	s_add_i32 s25, s2, 0x4400
	s_add_i32 s26, s2, 0x4800
	s_add_i32 s27, s2, 0x4c00
	s_add_i32 s28, s13, 0xc000
	s_add_i32 s29, s13, 0xc400
	s_add_i32 s30, s2, 0x10000
	s_add_i32 s31, s2, 0x10400
	s_add_i32 s33, s2, 0x10800
	s_add_i32 s34, s2, 0x10c00
	v_lshlrev_b32_e32 v15, 4, v5
	s_cmp_eq_u32 s18, 2
	v_mov_b32_e32 v19, 0
	v_ashrrev_i32_e32 v9, 31, v8
	s_cselect_b32 s2, s10, s19
	s_cselect_b32 s10, 11, 10
	v_bfe_u32 v89, v0, 4, 2
	v_xor_b32_e32 v14, v46, v0
	v_lshlrev_b64 v[8:9], s10, v[8:9]
	v_xor_b32_e32 v6, v89, v0
	s_cselect_b32 s3, s11, s20
	v_lshlrev_b64 v[22:23], 1, v[8:9]
	v_lshlrev_b32_e32 v12, 4, v6
	v_add_u32_e32 v6, s0, v13
	v_ashrrev_i32_e32 v7, 31, v6
	v_lshlrev_b64 v[10:11], s10, v[6:7]
	v_lshlrev_b64 v[20:21], 1, v[10:11]
	v_lshl_add_u64 v[8:9], s[2:3], 0, v[20:21]
	s_mov_b32 m0, s13
	v_mov_b32_e32 v50, v19
	v_mov_b32_e32 v51, v19
	v_mov_b32_e32 v52, v19
	v_mov_b32_e32 v53, v19
	v_mov_b32_e32 v48, v19
	v_mov_b32_e32 v49, v19
	v_mov_b32_e32 v54, v19
	v_mov_b32_e32 v55, v19
	v_mov_b32_e32 v56, v19
	v_mov_b32_e32 v57, v19
	v_mov_b32_e32 v58, v19
	v_mov_b32_e32 v59, v19
	v_mov_b32_e32 v60, v19
	v_mov_b32_e32 v61, v19
	v_mov_b32_e32 v62, v19
	s_waitcnt vmcnt(5)
	v_ashrrev_i32_e32 v3, 31, v2
	s_waitcnt vmcnt(4)
	v_ashrrev_i32_e32 v5, 31, v4
	v_lshlrev_b64 v[24:25], 12, v[2:3]
	v_lshlrev_b64 v[26:27], 12, v[4:5]
	s_waitcnt lgkmcnt(0)
	v_lshl_add_u64 v[2:3], s[4:5], 0, v[24:25]
	v_lshl_add_u64 v[4:5], s[4:5], 0, v[26:27]
	v_lshl_add_u64 v[28:29], v[2:3], 0, v[18:19]
	v_and_b32_e32 v18, 0x70, v15
	v_lshl_add_u64 v[30:31], v[4:5], 0, v[18:19]
	v_lshlrev_b32_e32 v4, 4, v14
	v_lshl_add_u64 v[2:3], s[2:3], 0, v[22:23]
	v_and_b32_e32 v4, 0x70, v4
	v_mov_b32_e32 v5, v19
	v_lshl_add_u64 v[34:35], v[2:3], 0, v[4:5]
	v_or_b32_e32 v2, 16, v6
	v_ashrrev_i32_e32 v3, 31, v2
	v_lshlrev_b64 v[2:3], s10, v[2:3]
	v_lshlrev_b64 v[36:37], 1, v[2:3]
	v_and_b32_e32 v18, 0x70, v12
	v_lshl_add_u64 v[2:3], s[2:3], 0, v[36:37]
	v_lshl_add_u64 v[38:39], v[2:3], 0, v[18:19]
	v_or_b32_e32 v2, 24, v13
	v_lshrrev_b32_e32 v47, 1, v2
	v_add_u32_e32 v2, s0, v2
	v_ashrrev_i32_e32 v3, 31, v2
	v_xor_b32_e32 v4, v47, v0
	v_lshlrev_b64 v[2:3], s10, v[2:3]
	v_lshlrev_b64 v[40:41], 1, v[2:3]
	v_lshlrev_b32_e32 v4, 4, v4
	v_lshl_add_u64 v[32:33], v[8:9], 0, v[18:19]
	v_lshl_add_u64 v[2:3], s[2:3], 0, v[40:41]
	v_and_b32_e32 v18, 0x70, v4
	v_lshl_add_u64 v[42:43], v[2:3], 0, v[18:19]
	v_and_b32_e32 v18, 48, v0
	global_load_dwordx4 v[14:17], v18, s[16:17]
	global_load_dwordx4 v[10:13], v18, s[16:17] offset:64
	global_load_dwordx4 v[6:9], v18, s[16:17] offset:128
	global_load_dwordx4 v[2:5], v18, s[16:17] offset:192
	s_nop 0
	global_load_lds_dwordx4 v[28:29], off
	s_mov_b32 m0, s21
	s_mov_b64 s[10:11], 0x80
	global_load_lds_dwordx4 v[30:31], off
	s_mov_b32 m0, s24
	v_lshl_add_u64 v[28:29], v[28:29], 0, s[10:11]
	global_load_lds_dwordx4 v[32:33], off
	s_mov_b32 m0, s25
	v_bfe_u32 v18, v0, 1, 3
	global_load_lds_dwordx4 v[34:35], off
	s_mov_b32 m0, s26
	s_mov_b64 s[16:17], 0x100
	global_load_lds_dwordx4 v[38:39], off
	s_mov_b32 m0, s27
	v_mov_b32_e32 v63, v19
	global_load_lds_dwordx4 v[42:43], off
	s_mov_b32 m0, s28
	v_mov_b32_e32 v64, v19
	global_load_lds_dwordx4 v[28:29], off
	v_lshl_add_u64 v[28:29], v[30:31], 0, s[10:11]
	s_mov_b32 m0, s29
	v_mov_b32_e32 v30, v19
	global_load_lds_dwordx4 v[28:29], off
	v_lshl_add_u64 v[28:29], v[32:33], 0, s[10:11]
	s_mov_b32 m0, s30
	v_mov_b32_e32 v31, v19
	global_load_lds_dwordx4 v[28:29], off
	v_lshl_add_u64 v[28:29], v[34:35], 0, s[10:11]
	s_mov_b32 m0, s31
	v_mov_b32_e32 v32, v19
	global_load_lds_dwordx4 v[28:29], off
	v_lshl_add_u64 v[28:29], v[38:39], 0, s[10:11]
	s_mov_b32 m0, s33
	v_mov_b32_e32 v33, v19
	global_load_lds_dwordx4 v[28:29], off
	v_lshl_add_u64 v[28:29], v[42:43], 0, s[10:11]
	s_mov_b32 m0, s34
	s_movk_i32 s10, 0xf00
	global_load_lds_dwordx4 v[28:29], off
	v_xor_b32_e32 v28, v89, v18
	v_bitop3_b32 v18, v89, v18, 4 bitop3:0x36
	v_lshlrev_b32_e32 v85, 4, v18
	v_bitop3_b32 v18, v47, 7, v0 bitop3:0x48
	v_lshl_or_b32 v40, v18, 4, v40
	v_bitop3_b32 v18, v89, 7, v0 bitop3:0x48
	v_lshlrev_b32_e32 v18, 4, v18
	v_lshlrev_b32_e32 v87, 4, v28
	v_lshl_add_u64 v[28:29], s[2:3], 0, v[40:41]
	v_or_b32_e32 v36, v36, v18
	v_lshl_add_u64 v[90:91], v[28:29], 0, s[16:17]
	v_lshl_add_u64 v[28:29], s[2:3], 0, v[36:37]
	v_or_b32_e32 v20, v20, v18
	v_bitop3_b32 v18, v45, 7, v0 bitop3:0x48
	v_lshl_add_u64 v[92:93], v[28:29], 0, s[16:17]
	v_bitop3_b32 v28, v46, 7, v0 bitop3:0x48
	v_lshl_add_u64 v[20:21], s[2:3], 0, v[20:21]
	v_lshl_or_b32 v26, v18, 4, v26
	v_bitop3_b32 v0, v44, 7, v0 bitop3:0x48
	v_lshl_or_b32 v22, v28, 4, v22
	v_lshl_add_u64 v[96:97], v[20:21], 0, s[16:17]
	v_lshl_add_u64 v[20:21], s[4:5], 0, v[26:27]
	v_lshl_or_b32 v24, v0, 4, v24
	v_lshl_add_u64 v[22:23], s[2:3], 0, v[22:23]
	v_lshl_add_u64 v[98:99], v[20:21], 0, s[16:17]
	v_lshl_add_u64 v[20:21], s[4:5], 0, v[24:25]
	s_cselect_b32 s10, s10, 0x700
	s_lshl_b32 s11, s23, 13
	s_lshl_b32 s13, s22, 13
	v_lshl_add_u64 v[94:95], v[22:23], 0, s[16:17]
	v_lshl_add_u64 v[100:101], v[20:21], 0, s[16:17]
	s_mov_b64 s[2:3], 0
	v_mov_b32_e32 v18, v19
	v_mov_b32_e32 v20, v19
	v_mov_b32_e32 v21, v19
	v_mov_b32_e32 v22, v19
	v_mov_b32_e32 v23, v19
	v_mov_b32_e32 v24, v19
	v_mov_b32_e32 v25, v19
	v_mov_b32_e32 v26, v19
	v_mov_b32_e32 v27, v19
	v_mov_b32_e32 v28, v19
	v_mov_b32_e32 v29, v19
	v_mov_b32_e32 v38, v19
	v_mov_b32_e32 v39, v19
	v_mov_b32_e32 v40, v19
	v_mov_b32_e32 v41, v19
	v_mov_b32_e32 v42, v19
	v_mov_b32_e32 v43, v19
	v_mov_b32_e32 v44, v19
	v_mov_b32_e32 v45, v19
	v_mov_b32_e32 v46, v19
	v_mov_b32_e32 v47, v19
	v_mov_b32_e32 v65, v19
	v_mov_b32_e32 v66, v19
	v_mov_b32_e32 v67, v19
	v_mov_b32_e32 v68, v19
	v_mov_b32_e32 v69, v19
	v_mov_b32_e32 v70, v19
	v_mov_b32_e32 v71, v19
	v_mov_b32_e32 v72, v19
	v_mov_b32_e32 v73, v19
	v_mov_b32_e32 v74, v19
	v_mov_b32_e32 v75, v19
	v_mov_b32_e32 v76, v19
	v_mov_b32_e32 v77, v19
	v_mov_b32_e32 v34, v19
	v_mov_b32_e32 v35, v19
	v_mov_b32_e32 v36, v19
	v_mov_b32_e32 v37, v19
	v_mov_b32_e32 v78, v19
	v_mov_b32_e32 v79, v19
	v_mov_b32_e32 v80, v19
	v_mov_b32_e32 v81, v19
	v_lshlrev_b32_e32 v0, 2, v89
	v_lshlrev_b32_e32 v89, 7, v1

.LBB2_12:
	s_or_b64 exec, exec, s[0:1]
	v_or_b32_e32 v34, 48, v83
	v_cmp_gt_u32_e32 vcc, s2, v34
	s_mov_b64 s[0:1], exec
	s_cbranch_execz .LBB2_14
	v_add_f32_e32 v15, v15, v27
	v_ashrrev_i32_e32 v83, 31, v82
	v_add_f32_e32 v14, v14, v26
	v_max_f32_e32 v26, 0, v15
	v_add_f32_e32 v15, v16, v28
	v_add_f32_e32 v16, v17, v29
	v_lshlrev_b64 v[34:35], 11, v[82:83]
	v_max_f32_e32 v14, 0, v14
	v_max_f32_e32 v15, 0, v15
	v_max_f32_e32 v16, 0, v16
	v_lshl_add_u64 v[0:1], v[0:1], 0, v[34:35]
	v_cvt_pk_f16_f32 v15, v15, v16
	v_cvt_pk_f16_f32 v14, v14, v26
	v_add_f32_e32 v11, v11, v23
	ds_write_b64 v161, v[14:15]
	v_add_f32_e32 v10, v10, v22
	v_max_f32_e32 v14, 0, v11
	v_add_f32_e32 v11, v12, v24
	v_add_f32_e32 v12, v13, v25
	v_max_f32_e32 v10, 0, v10
	v_max_f32_e32 v11, 0, v11
	v_max_f32_e32 v12, 0, v12
	v_cvt_pk_f16_f32 v11, v11, v12
	v_cvt_pk_f16_f32 v10, v10, v14
	v_add_f32_e32 v7, v7, v19
	ds_write_b64 v161, v[10:11] offset:32
	v_add_f32_e32 v6, v6, v18
	v_max_f32_e32 v10, 0, v7
	v_add_f32_e32 v7, v8, v20
	v_add_f32_e32 v8, v9, v21
	v_max_f32_e32 v6, 0, v6
	v_max_f32_e32 v7, 0, v7
	v_max_f32_e32 v8, 0, v8
	v_cvt_pk_f16_f32 v7, v7, v8
	v_cvt_pk_f16_f32 v6, v6, v10
	v_add_f32_e32 v3, v3, v31
	ds_write_b64 v161, v[6:7] offset:64
	v_add_f32_e32 v2, v2, v30
	v_max_f32_e32 v6, 0, v3
	v_add_f32_e32 v3, v4, v32
	v_add_f32_e32 v4, v5, v33
	v_max_f32_e32 v2, 0, v2
	v_max_f32_e32 v3, 0, v3
	v_max_f32_e32 v4, 0, v4
	v_cvt_pk_f16_f32 v3, v3, v4
	v_cvt_pk_f16_f32 v2, v2, v6
	ds_write_b64 v161, v[2:3] offset:96
	s_waitcnt lgkmcnt(4)
	v_lshl_add_u64 v[178:179], v[178:179], 0, v[182:183]
	v_lshl_add_u64 v[180:181], v[180:181], 0, v[182:183]
	s_mov_b64 s[42:43], exec
	s_and_b64 exec, s[42:43], s[38:39]
	global_store_dwordx4 v[178:179], v[170:173], off sc1
	s_and_b64 exec, s[42:43], s[40:41]
	global_store_dwordx4 v[180:181], v[174:177], off sc1
	s_mov_b64 exec, s[42:43]
	ds_read_b128 v[170:173], v164
	ds_read_b128 v[174:177], v164 offset:1152
	ds_bpermute_b32 v178, v165, v0
	ds_bpermute_b32 v179, v165, v1
	ds_bpermute_b32 v180, v166, v0
	ds_bpermute_b32 v181, v166, v1
	v_add_u32_e32 v184, 48, v167
	v_cmp_gt_u32_e64 s[38:39], s2, v184
	v_add_u32_e32 v184, 8, v184
	v_cmp_gt_u32_e64 s[40:41], s2, v184
	s_waitcnt lgkmcnt(0)
	v_lshl_add_u64 v[178:179], v[178:179], 0, v[182:183]
	v_lshl_add_u64 v[180:181], v[180:181], 0, v[182:183]
	s_mov_b64 s[42:43], exec
	s_and_b64 exec, s[42:43], s[38:39]
	global_store_dwordx4 v[178:179], v[170:173], off sc1
	s_and_b64 exec, s[42:43], s[40:41]
	global_store_dwordx4 v[180:181], v[174:177], off sc1
	s_mov_b64 exec, s[42:43]
	s_cmp_lg_u32 s47, 0
	s_cbranch_scc1 .LBB2_14
	s_cmp_gt_u32 s46, 0xff
	s_cbranch_scc1 .LBB2_14
	s_mov_b32 s47, 1
	s_waitcnt lgkmcnt(0)
	s_barrier
	s_mov_b64 s[0:1], s[44:45]
	s_add_u32 s2, s46, 0x100
	v_mov_b32_e32 v0, v186
	s_mov_b64 s[4:5], -1
	s_branch .LBB2_2

	.amdhsa_kernel _Z16gemm_glds_kernelILi2EEvPKDF16_PDF16_PKiS4_S1_S1_PKfiS6_Pc
		.amdhsa_group_segment_fixed_size 0
		.amdhsa_private_segment_fixed_size 0
		.amdhsa_kernarg_size 80
		.amdhsa_user_sgpr_count 2
		.amdhsa_user_sgpr_dispatch_ptr 0
		.amdhsa_user_sgpr_queue_ptr 0
		.amdhsa_user_sgpr_kernarg_segment_ptr 1
		.amdhsa_user_sgpr_dispatch_id 0
		.amdhsa_user_sgpr_kernarg_preload_length 0
		.amdhsa_user_sgpr_kernarg_preload_offset 0
		.amdhsa_user_sgpr_private_segment_size 0
		.amdhsa_uses_dynamic_stack 0
		.amdhsa_enable_private_segment 0
		.amdhsa_system_sgpr_workgroup_id_x 1
		.amdhsa_system_sgpr_workgroup_id_y 0
		.amdhsa_system_sgpr_workgroup_id_z 0
		.amdhsa_system_sgpr_workgroup_info 0
		.amdhsa_system_vgpr_workitem_id 0
		.amdhsa_next_free_vgpr 188
		.amdhsa_next_free_sgpr 48
		.amdhsa_accum_offset 188
		.amdhsa_reserve_vcc 1
		.amdhsa_float_round_mode_32 0
		.amdhsa_float_round_mode_16_64 0
		.amdhsa_float_denorm_mode_32 3
		.amdhsa_float_denorm_mode_16_64 3
		.amdhsa_dx10_clamp 1
		.amdhsa_ieee_mode 1
		.amdhsa_fp16_overflow 0
		.amdhsa_tg_split 0
		.amdhsa_exception_fp_ieee_invalid_op 0
		.amdhsa_exception_fp_denorm_src 0
		.amdhsa_exception_fp_ieee_div_zero 0
		.amdhsa_exception_fp_ieee_overflow 0
		.amdhsa_exception_fp_ieee_underflow 0
		.amdhsa_exception_fp_ieee_inexact 0
		.amdhsa_exception_int_div_zero 0
	.end_amdhsa_kernel

amdhsa.kernels:
  - .agpr_count:     0
    .args:
      - .actual_access:  read_only
        .address_space:  global
        .offset:         0
        .size:           8
        .value_kind:     global_buffer
      - .actual_access:  read_only
        .address_space:  global
        .offset:         8
        .size:           8
        .value_kind:     global_buffer
      - .actual_access:  read_only
        .address_space:  global
        .offset:         16
        .size:           8
        .value_kind:     global_buffer
      - .actual_access:  read_only
        .address_space:  global
        .offset:         24
        .size:           8
        .value_kind:     global_buffer
      - .actual_access:  read_only
        .address_space:  global
        .offset:         32
        .size:           8
        .value_kind:     global_buffer
      - .actual_access:  read_only
        .address_space:  global
        .offset:         40
        .size:           8
        .value_kind:     global_buffer
      - .actual_access:  read_only
        .address_space:  global
        .offset:         48
        .size:           8
        .value_kind:     global_buffer
      - .actual_access:  read_only
        .address_space:  global
        .offset:         56
        .size:           8
        .value_kind:     global_buffer
      - .actual_access:  write_only
        .address_space:  global
        .offset:         64
        .size:           8
        .value_kind:     global_buffer
    .group_segment_fixed_size: 16832
    .kernarg_segment_align: 8
    .kernarg_segment_size: 72
    .language:       OpenCL C
    .language_version:
      - 2
      - 0
    .max_flat_workgroup_size: 256
    .name:           _Z12front_kernelPKiS0_S0_PKfS2_S2_S2_S2_Pc
    .private_segment_fixed_size: 0
    .sgpr_count:     106
    .sgpr_spill_count: 398
    .symbol:         _Z12front_kernelPKiS0_S0_PKfS2_S2_S2_S2_Pc.kd
    .uniform_work_group_size: 1
    .uses_dynamic_stack: false
    .vgpr_count:     78
    .vgpr_spill_count: 0
    .wavefront_size: 64
  - .agpr_count:     0
    .args:
      - .actual_access:  read_only
        .address_space:  global
        .offset:         0
        .size:           8
        .value_kind:     global_buffer
      - .actual_access:  read_only
        .address_space:  global
        .offset:         8
        .size:           8
        .value_kind:     global_buffer
      - .actual_access:  read_only
        .address_space:  global
        .offset:         16
        .size:           8
        .value_kind:     global_buffer
      - .actual_access:  write_only
        .address_space:  global
        .offset:         24
        .size:           8
        .value_kind:     global_buffer
    .group_segment_fixed_size: 0
    .kernarg_segment_align: 8
    .kernarg_segment_size: 32
    .language:       OpenCL C
    .language_version:
      - 2
      - 0
    .max_flat_workgroup_size: 256
    .name:           _Z12final_kernelPKDF16_PKfS2_Pf
    .private_segment_fixed_size: 0
    .sgpr_count:     14
    .sgpr_spill_count: 0
    .symbol:         _Z12final_kernelPKDF16_PKfS2_Pf.kd
    .uniform_work_group_size: 1
    .uses_dynamic_stack: false
    .vgpr_count:     40
    .vgpr_spill_count: 0
    .wavefront_size: 64
  - .agpr_count:     0
    .args:
      - .address_space:  global
        .offset:         0
        .size:           8
        .value_kind:     global_buffer
      - .actual_access:  write_only
        .address_space:  global
        .offset:         8
        .size:           8
        .value_kind:     global_buffer
      - .actual_access:  read_only
        .address_space:  global
        .offset:         16
        .size:           8
        .value_kind:     global_buffer
      - .actual_access:  read_only
        .address_space:  global
        .offset:         24
        .size:           8
        .value_kind:     global_buffer
      - .address_space:  global
        .offset:         32
        .size:           8
        .value_kind:     global_buffer
      - .address_space:  global
        .offset:         40
        .size:           8
        .value_kind:     global_buffer
      - .actual_access:  read_only
        .address_space:  global
        .offset:         48
        .size:           8
        .value_kind:     global_buffer
      - .offset:         56
        .size:           4
        .value_kind:     by_value
      - .actual_access:  read_only
        .address_space:  global
        .offset:         64
        .size:           8
        .value_kind:     global_buffer
      - .actual_access:  write_only
        .address_space:  global
        .offset:         72
        .size:           8
        .value_kind:     global_buffer
    .group_segment_fixed_size: 0
    .kernarg_segment_align: 8
    .kernarg_segment_size: 80
    .language:       OpenCL C
    .language_version:
      - 2
      - 0
    .max_flat_workgroup_size: 512
    .name:           _Z16gemm_glds_kernelILi2EEvPKDF16_PDF16_PKiS4_S1_S1_PKfiS6_Pc
    .private_segment_fixed_size: 0
    .sgpr_count:     50
    .sgpr_spill_count: 0
    .symbol:         _Z16gemm_glds_kernelILi2EEvPKDF16_PDF16_PKiS4_S1_S1_PKfiS6_Pc.kd
    .uniform_work_group_size: 1
    .uses_dynamic_stack: false
    .vgpr_count:     188
    .vgpr_spill_count: 0
    .wavefront_size: 64
  - .agpr_count:     0
    .args:
      - .actual_access:  read_only
        .address_space:  global
        .offset:         0
        .size:           8
        .value_kind:     global_buffer
      - .actual_access:  write_only
        .address_space:  global
        .offset:         8
        .size:           8
        .value_kind:     global_buffer
      - .actual_access:  read_only
        .address_space:  global
        .offset:         16
        .size:           8
        .value_kind:     global_buffer
      - .actual_access:  read_only
        .address_space:  global
        .offset:         24
        .size:           8
        .value_kind:     global_buffer
      - .actual_access:  read_only
        .address_space:  global
        .offset:         32
        .size:           8
        .value_kind:     global_buffer
      - .actual_access:  read_only
        .address_space:  global
        .offset:         40
        .size:           8
        .value_kind:     global_buffer
      - .actual_access:  read_only
        .address_space:  global
        .offset:         48
        .size:           8
        .value_kind:     global_buffer
    .group_segment_fixed_size: 0
    .kernarg_segment_align: 8
    .kernarg_segment_size: 56
    .language:       OpenCL C
    .language_version:
      - 2
      - 0
    .max_flat_workgroup_size: 512
    .name:           _Z11gemm_kernelILi0ELi192ELi256ELi128ELi2ELi4ELi2ELi2ELi64EEvPKDF16_PDF16_PKiS4_S1_S1_PKf
    .private_segment_fixed_size: 0
    .sgpr_count:     30
    .sgpr_spill_count: 0
    .symbol:         _Z11gemm_kernelILi0ELi192ELi256ELi128ELi2ELi4ELi2ELi2ELi64EEvPKDF16_PDF16_PKiS4_S1_S1_PKf.kd
    .uniform_work_group_size: 1
    .uses_dynamic_stack: false
    .vgpr_count:     254
    .vgpr_spill_count: 0
    .wavefront_size: 64
  - .agpr_count:     0
    .args:
      - .actual_access:  read_only
        .address_space:  global
        .offset:         0
        .size:           8
        .value_kind:     global_buffer
      - .actual_access:  write_only
        .address_space:  global
        .offset:         8
        .size:           8
        .value_kind:     global_buffer
      - .actual_access:  read_only
        .address_space:  global
        .offset:         16
        .size:           8
        .value_kind:     global_buffer
      - .actual_access:  read_only
        .address_space:  global
        .offset:         24
        .size:           8
        .value_kind:     global_buffer
      - .actual_access:  read_only
        .address_space:  global
        .offset:         32
        .size:           8
        .value_kind:     global_buffer
      - .actual_access:  read_only
        .address_space:  global
        .offset:         40
        .size:           8
        .value_kind:     global_buffer
      - .actual_access:  read_only
        .address_space:  global
        .offset:         48
        .size:           8
        .value_kind:     global_buffer
    .group_segment_fixed_size: 0
    .kernarg_segment_align: 8
    .kernarg_segment_size: 56
    .language:       OpenCL C
    .language_version:
      - 2
      - 0
    .max_flat_workgroup_size: 512
    .name:           _Z11gemm_kernelILi0ELi96ELi256ELi128ELi2ELi4ELi2ELi2ELi64EEvPKDF16_PDF16_PKiS4_S1_S1_PKf
    .private_segment_fixed_size: 0
    .sgpr_count:     32
    .sgpr_spill_count: 0
    .symbol:         _Z11gemm_kernelILi0ELi96ELi256ELi128ELi2ELi4ELi2ELi2ELi64EEvPKDF16_PDF16_PKiS4_S1_S1_PKf.kd
    .uniform_work_group_size: 1
    .uses_dynamic_stack: false
    .vgpr_count:     224
    .vgpr_spill_count: 0
    .wavefront_size: 64
  - .agpr_count:     0
    .args:
      - .address_space:  global
        .offset:         0
        .size:           8
        .value_kind:     global_buffer
      - .actual_access:  write_only
        .address_space:  global
        .offset:         8
        .size:           8
        .value_kind:     global_buffer
      - .actual_access:  read_only
        .address_space:  global
        .offset:         16
        .size:           8
        .value_kind:     global_buffer
      - .actual_access:  read_only
        .address_space:  global
        .offset:         24
        .size:           8
        .value_kind:     global_buffer
      - .address_space:  global
        .offset:         32
        .size:           8
        .value_kind:     global_buffer
      - .address_space:  global
        .offset:         40
        .size:           8
        .value_kind:     global_buffer
      - .actual_access:  read_only
        .address_space:  global
        .offset:         48
        .size:           8
        .value_kind:     global_buffer
    .group_segment_fixed_size: 0
    .kernarg_segment_align: 8
    .kernarg_segment_size: 56
    .language:       OpenCL C
    .language_version:
      - 2
      - 0
    .max_flat_workgroup_size: 256
    .name:           _Z15gemm_dma_kernelILi0ELi96ELi128ELi64ELi2ELi2ELi3EEvPKDF16_PDF16_PKiS4_S1_S1_PKf
    .private_segment_fixed_size: 0
    .sgpr_count:     33
    .sgpr_spill_count: 0
    .symbol:         _Z15gemm_dma_kernelILi0ELi96ELi128ELi64ELi2ELi2ELi3EEvPKDF16_PDF16_PKiS4_S1_S1_PKf.kd
    .uniform_work_group_size: 1
    .uses_dynamic_stack: false
    .vgpr_count:     224
    .vgpr_spill_count: 0
    .wavefront_size: 64
  - .agpr_count:     0
    .args:
      - .actual_access:  read_only
        .address_space:  global
        .offset:         0
        .size:           8
        .value_kind:     global_buffer
      - .actual_access:  write_only
        .address_space:  global
        .offset:         8
        .size:           8
        .value_kind:     global_buffer
      - .actual_access:  read_only
        .address_space:  global
        .offset:         16
        .size:           8
        .value_kind:     global_buffer
      - .actual_access:  read_only
        .address_space:  global
        .offset:         24
        .size:           8
        .value_kind:     global_buffer
      - .actual_access:  read_only
        .address_space:  global
        .offset:         32
        .size:           8
        .value_kind:     global_buffer
      - .actual_access:  read_only
        .address_space:  global
        .offset:         40
        .size:           8
        .value_kind:     global_buffer
      - .actual_access:  read_only
        .address_space:  global
        .offset:         48
        .size:           8
        .value_kind:     global_buffer
    .group_segment_fixed_size: 0
    .kernarg_segment_align: 8
    .kernarg_segment_size: 56
    .language:       OpenCL C
    .language_version:
      - 2
      - 0
    .max_flat_workgroup_size: 256
    .name:           _Z11gemm_kernelILi0ELi48ELi128ELi64ELi1ELi4ELi2ELi2ELi128EEvPKDF16_PDF16_PKiS4_S1_S1_PKf
    .private_segment_fixed_size: 0
    .sgpr_count:     30
    .sgpr_spill_count: 0
    .symbol:         _Z11gemm_kernelILi0ELi48ELi128ELi64ELi1ELi4ELi2ELi2ELi128EEvPKDF16_PDF16_PKiS4_S1_S1_PKf.kd
    .uniform_work_group_size: 1
    .uses_dynamic_stack: false
    .vgpr_count:     224
    .vgpr_spill_count: 0
    .wavefront_size: 64
  - .agpr_count:     0
    .args:
      - .actual_access:  read_only
        .address_space:  global
        .offset:         0
        .size:           8
        .value_kind:     global_buffer
      - .actual_access:  write_only
        .address_space:  global
        .offset:         8
        .size:           8
        .value_kind:     global_buffer
      - .actual_access:  read_only
        .address_space:  global
        .offset:         16
        .size:           8
        .value_kind:     global_buffer
      - .actual_access:  read_only
        .address_space:  global
        .offset:         24
        .size:           8
        .value_kind:     global_buffer
      - .actual_access:  read_only
        .address_space:  global
        .offset:         32
        .size:           8
        .value_kind:     global_buffer
      - .actual_access:  read_only
        .address_space:  global
        .offset:         40
        .size:           8
        .value_kind:     global_buffer
      - .actual_access:  read_only
        .address_space:  global
        .offset:         48
        .size:           8
        .value_kind:     global_buffer
    .group_segment_fixed_size: 0
    .kernarg_segment_align: 8
    .kernarg_segment_size: 56
    .language:       OpenCL C
    .language_version:
      - 2
      - 0
    .max_flat_workgroup_size: 512
    .name:           _Z11gemm_kernelILi1ELi64ELi128ELi128ELi2ELi4ELi2ELi2ELi128EEvPKDF16_PDF16_PKiS4_S1_S1_PKf
    .private_segment_fixed_size: 0
    .sgpr_count:     23
    .sgpr_spill_count: 0
    .symbol:         _Z11gemm_kernelILi1ELi64ELi128ELi128ELi2ELi4ELi2ELi2ELi128EEvPKDF16_PDF16_PKiS4_S1_S1_PKf.kd
    .uniform_work_group_size: 1
    .uses_dynamic_stack: false
    .vgpr_count:     224
    .vgpr_spill_count: 0
    .wavefront_size: 64
